# moe_cvt: hand-written item loop (fixed tile position per wave, constant address strides, ~90 instr/item) with five register sets = four items' loads in flight (on top of v30)
# speedup vs baseline: 1.0071x; 1.0071x over previous
.LBB0_1232:
	s_waitcnt vmcnt(0)
	v_mbcnt_lo_u32_b32 v66, -1, 0
	v_mbcnt_hi_u32_b32 v66, -1, v66
	s_waitcnt vmcnt(0)
	v_add_u32_e32 v0, s15, v66
	s_barrier
	v_readfirstlane_b32 s0, v0
	s_ashr_i32 s30, s0, 6
	v_readlane_b32 s0, v253, 52
	s_add_i32 s12, s30, s0
	s_cmp_gt_i32 s12, 0xbfff
	s_cbranch_scc1 .LBB0_1074
	v_and_b32_e32 v119, 7, v66
	v_lshrrev_b32_e32 v120, 3, v66
	s_mulk_i32 s30, 0x2100
	v_mul_u32_u24_e32 v121, 33, v120
	v_lshl_add_u32 v121, v119, 2, v121
	v_lshl_add_u32 v106, v121, 2, s30
	v_add_u32_e32 v107, 0x420, v106
	v_add_u32_e32 v108, 0x840, v106
	v_add_u32_e32 v109, 0xc60, v106
	v_add_u32_e32 v110, 0x1080, v106
	v_add_u32_e32 v111, 0x14a0, v106
	v_add_u32_e32 v112, 0x18c0, v106
	v_add_u32_e32 v113, 0x1ce0, v106
	v_mul_u32_u24_e32 v121, 0x108, v119
	v_add_u32_e32 v121, v121, v120
	v_lshl_add_u32 v114, v121, 2, s30
	s_mov_b32 s26, 0x42800000
	s_mov_b32 s27, 0x42800000
	s_mov_b32 s13, 0x1000000
	s_mov_b32 s23, 0x400000
	s_mov_b32 s29, 0
	s_lshr_b32 s0, s12, 10
	s_add_i32 s0, s0, s46
	s_mov_b32 s1, 0
	v_readlane_b32 s34, v254, 29
	v_readlane_b32 s35, v254, 30
	s_lshl_b64 s[36:37], s[0:1], 23
	s_add_u32 s6, s34, s36
	s_addc_u32 s7, s35, s37
	s_bfe_u32 s31, s12, 0x40006
	s_lshl_b32 s36, s31, 19
	s_add_u32 s6, s6, s36
	s_addc_u32 s7, s7, 0
	s_and_b32 s38, s12, 63
	s_lshl_b32 s36, s38, 7
	s_add_u32 s6, s6, s36
	s_addc_u32 s7, s7, 0
	s_lshl_b64 s[36:37], s[0:1], 21
	s_add_u32 s8, s49, s36
	s_addc_u32 s9, s50, s37
	s_lshl_b32 s36, s38, 15
	s_add_u32 s8, s8, s36
	s_addc_u32 s9, s9, 0
	s_lshl_b32 s36, s31, 6
	s_add_u32 s8, s8, s36
	s_addc_u32 s9, s9, 0
	s_mov_b32 s10, 16
	v_lshlrev_b32_e32 v121, 13, v120
	v_lshl_add_u32 v98, v119, 4, v121
	v_add_u32_e32 v99, 0x10000, v98
	v_add_u32_e32 v100, 0x20000, v98
	v_add_u32_e32 v101, 0x30000, v98
	v_add_u32_e32 v102, 0x40000, v98
	v_add_u32_e32 v103, 0x50000, v98
	v_add_u32_e32 v104, 0x60000, v98
	v_add_u32_e32 v105, 0x70000, v98
	v_and_b32_e32 v121, 1, v120
	v_lshlrev_b32_e32 v121, 2, v121
	v_lshrrev_b32_e32 v122, 1, v120
	v_or_b32_e32 v121, v121, v122
	v_lshlrev_b32_e32 v121, 10, v121
	v_lshl_add_u32 v115, v119, 3, v121
	v_add_u32_e32 v116, 0x2000, v115
	v_add_u32_e32 v117, 0x4000, v115
	v_add_u32_e32 v118, 0x6000, v115
	s_branch .Lcvt_run
.Lcvt_phase1:
	s_mov_b32 s29, 1
	s_lshr_b32 s0, s12, 9
	s_add_i32 s0, s0, s46
	s_mov_b32 s1, 0
	v_readlane_b32 s34, v254, 31
	v_readlane_b32 s35, v254, 32
	s_lshl_b64 s[36:37], s[0:1], 22
	s_add_u32 s6, s34, s36
	s_addc_u32 s7, s35, s37
	s_bfe_u32 s31, s12, 0x40005
	s_lshl_b32 s36, s31, 18
	s_add_u32 s6, s6, s36
	s_addc_u32 s7, s7, 0
	s_and_b32 s38, s12, 31
	s_lshl_b32 s36, s38, 7
	s_add_u32 s6, s6, s36
	s_addc_u32 s7, s7, 0
	s_lshl_b64 s[36:37], s[0:1], 20
	s_add_u32 s8, s47, s36
	s_addc_u32 s9, s48, s37
	s_lshl_b32 s36, s38, 15
	s_add_u32 s8, s8, s36
	s_addc_u32 s9, s9, 0
	s_lshl_b32 s36, s31, 6
	s_add_u32 s8, s8, s36
	s_addc_u32 s9, s9, 0
	s_mov_b32 s10, 8
	v_lshlrev_b32_e32 v121, 12, v120
	v_lshl_add_u32 v98, v119, 4, v121
	v_add_u32_e32 v99, 0x8000, v98
	v_add_u32_e32 v100, 0x10000, v98
	v_add_u32_e32 v101, 0x18000, v98
	v_add_u32_e32 v102, 0x20000, v98
	v_add_u32_e32 v103, 0x28000, v98
	v_add_u32_e32 v104, 0x30000, v98
	v_add_u32_e32 v105, 0x38000, v98
	v_lshlrev_b32_e32 v121, 10, v120
	v_lshl_add_u32 v115, v119, 3, v121
	v_add_u32_e32 v116, 0x2000, v115
	v_add_u32_e32 v117, 0x4000, v115
	v_add_u32_e32 v118, 0x6000, v115
.Lcvt_run:
	s_add_i32 s11, s10, -1
	global_load_dwordx4 v[2:5], v98, s[6:7]
	global_load_dwordx4 v[6:9], v99, s[6:7]
	global_load_dwordx4 v[10:13], v100, s[6:7]
	global_load_dwordx4 v[14:17], v101, s[6:7]
	global_load_dwordx4 v[18:21], v102, s[6:7]
	global_load_dwordx4 v[22:25], v103, s[6:7]
	global_load_dwordx4 v[26:29], v104, s[6:7]
	global_load_dwordx4 v[30:33], v105, s[6:7]
	s_cmp_lg_u32 s11, 0
	s_cselect_b32 s0, s13, 0
	s_cselect_b32 s1, 1, 0
	s_add_u32 s6, s6, s0
	s_addc_u32 s7, s7, 0
	s_sub_u32 s11, s11, s1
	global_load_dwordx4 v[34:37], v98, s[6:7]
	global_load_dwordx4 v[38:41], v99, s[6:7]
	global_load_dwordx4 v[42:45], v100, s[6:7]
	global_load_dwordx4 v[46:49], v101, s[6:7]
	global_load_dwordx4 v[50:53], v102, s[6:7]
	global_load_dwordx4 v[54:57], v103, s[6:7]
	global_load_dwordx4 v[58:61], v104, s[6:7]
	global_load_dwordx4 v[62:65], v105, s[6:7]
	s_cmp_lg_u32 s11, 0
	s_cselect_b32 s0, s13, 0
	s_cselect_b32 s1, 1, 0
	s_add_u32 s6, s6, s0
	s_addc_u32 s7, s7, 0
	s_sub_u32 s11, s11, s1
	global_load_dwordx4 v[66:69], v98, s[6:7]
	global_load_dwordx4 v[70:73], v99, s[6:7]
	global_load_dwordx4 v[74:77], v100, s[6:7]
	global_load_dwordx4 v[78:81], v101, s[6:7]
	global_load_dwordx4 v[82:85], v102, s[6:7]
	global_load_dwordx4 v[86:89], v103, s[6:7]
	global_load_dwordx4 v[90:93], v104, s[6:7]
	global_load_dwordx4 v[94:97], v105, s[6:7]
	s_cmp_lg_u32 s11, 0
	s_cselect_b32 s0, s13, 0
	s_cselect_b32 s1, 1, 0
	s_add_u32 s6, s6, s0
	s_addc_u32 s7, s7, 0
	s_sub_u32 s11, s11, s1
	global_load_dwordx4 v[124:127], v98, s[6:7]
	global_load_dwordx4 v[128:131], v99, s[6:7]
	global_load_dwordx4 v[132:135], v100, s[6:7]
	global_load_dwordx4 v[136:139], v101, s[6:7]
	global_load_dwordx4 v[140:143], v102, s[6:7]
	global_load_dwordx4 v[144:147], v103, s[6:7]
	global_load_dwordx4 v[148:151], v104, s[6:7]
	global_load_dwordx4 v[152:155], v105, s[6:7]
	s_cmp_lg_u32 s11, 0
	s_cselect_b32 s0, s13, 0
	s_cselect_b32 s1, 1, 0
	s_add_u32 s6, s6, s0
	s_addc_u32 s7, s7, 0
	s_sub_u32 s11, s11, s1
.Lcvt_loop:
	global_load_dwordx4 v[156:159], v98, s[6:7]
	global_load_dwordx4 v[160:163], v99, s[6:7]
	global_load_dwordx4 v[164:167], v100, s[6:7]
	global_load_dwordx4 v[168:171], v101, s[6:7]
	global_load_dwordx4 v[172:175], v102, s[6:7]
	global_load_dwordx4 v[176:179], v103, s[6:7]
	global_load_dwordx4 v[180:183], v104, s[6:7]
	global_load_dwordx4 v[184:187], v105, s[6:7]
	s_cmp_lg_u32 s11, 0
	s_cselect_b32 s0, s13, 0
	s_cselect_b32 s1, 1, 0
	s_add_u32 s6, s6, s0
	s_addc_u32 s7, s7, 0
	s_sub_u32 s11, s11, s1
	s_waitcnt vmcnt(32)
	ds_write2_b32 v106, v2, v3 offset1:1
	ds_write2_b32 v106, v4, v5 offset0:2 offset1:3
	ds_write2_b32 v107, v6, v7 offset1:1
	ds_write2_b32 v107, v8, v9 offset0:2 offset1:3
	ds_write2_b32 v108, v10, v11 offset1:1
	ds_write2_b32 v108, v12, v13 offset0:2 offset1:3
	ds_write2_b32 v109, v14, v15 offset1:1
	ds_write2_b32 v109, v16, v17 offset0:2 offset1:3
	ds_write2_b32 v110, v18, v19 offset1:1
	ds_write2_b32 v110, v20, v21 offset0:2 offset1:3
	ds_write2_b32 v111, v22, v23 offset1:1
	ds_write2_b32 v111, v24, v25 offset0:2 offset1:3
	ds_write2_b32 v112, v26, v27 offset1:1
	ds_write2_b32 v112, v28, v29 offset0:2 offset1:3
	ds_write2_b32 v113, v30, v31 offset1:1
	ds_write2_b32 v113, v32, v33 offset0:2 offset1:3
	s_waitcnt lgkmcnt(0)
	ds_read2_b32 v[2:3], v114 offset1:33
	ds_read2_b32 v[4:5], v114 offset0:66 offset1:99
	ds_read2_b32 v[6:7], v114 offset0:132 offset1:165
	ds_read2_b32 v[8:9], v114 offset0:198 offset1:231
	ds_read2_b32 v[10:11], v114 offset0:8 offset1:41
	ds_read2_b32 v[12:13], v114 offset0:74 offset1:107
	ds_read2_b32 v[14:15], v114 offset0:140 offset1:173
	ds_read2_b32 v[16:17], v114 offset0:206 offset1:239
	ds_read2_b32 v[18:19], v114 offset0:16 offset1:49
	ds_read2_b32 v[20:21], v114 offset0:82 offset1:115
	ds_read2_b32 v[22:23], v114 offset0:148 offset1:181
	ds_read2_b32 v[24:25], v114 offset0:214 offset1:247
	ds_read2_b32 v[26:27], v114 offset0:24 offset1:57
	ds_read2_b32 v[28:29], v114 offset0:90 offset1:123
	ds_read2_b32 v[30:31], v114 offset0:156 offset1:189
	ds_read2_b32 v[32:33], v114 offset0:222 offset1:255
	s_waitcnt lgkmcnt(12)
	v_pk_mul_f32 v[2:3], v[2:3], s[26:27] op_sel_hi:[1,0]
	v_pk_mul_f32 v[4:5], v[4:5], s[26:27] op_sel_hi:[1,0]
	v_pk_mul_f32 v[6:7], v[6:7], s[26:27] op_sel_hi:[1,0]
	v_pk_mul_f32 v[8:9], v[8:9], s[26:27] op_sel_hi:[1,0]
	v_cvt_pk_fp8_f32 v2, v2, v3
	v_cvt_pk_fp8_f32 v3, v6, v7
	v_cvt_pk_fp8_f32 v2, v4, v5 op_sel:[0,0,1]
	v_cvt_pk_fp8_f32 v3, v8, v9 op_sel:[0,0,1]
	s_nop 1
	global_store_dwordx2 v115, v[2:3], s[8:9]
	s_waitcnt lgkmcnt(8)
	v_pk_mul_f32 v[10:11], v[10:11], s[26:27] op_sel_hi:[1,0]
	v_pk_mul_f32 v[12:13], v[12:13], s[26:27] op_sel_hi:[1,0]
	v_pk_mul_f32 v[14:15], v[14:15], s[26:27] op_sel_hi:[1,0]
	v_pk_mul_f32 v[16:17], v[16:17], s[26:27] op_sel_hi:[1,0]
	v_cvt_pk_fp8_f32 v10, v10, v11
	v_cvt_pk_fp8_f32 v11, v14, v15
	v_cvt_pk_fp8_f32 v10, v12, v13 op_sel:[0,0,1]
	v_cvt_pk_fp8_f32 v11, v16, v17 op_sel:[0,0,1]
	s_nop 1
	global_store_dwordx2 v116, v[10:11], s[8:9]
	s_waitcnt lgkmcnt(4)
	v_pk_mul_f32 v[18:19], v[18:19], s[26:27] op_sel_hi:[1,0]
	v_pk_mul_f32 v[20:21], v[20:21], s[26:27] op_sel_hi:[1,0]
	v_pk_mul_f32 v[22:23], v[22:23], s[26:27] op_sel_hi:[1,0]
	v_pk_mul_f32 v[24:25], v[24:25], s[26:27] op_sel_hi:[1,0]
	v_cvt_pk_fp8_f32 v18, v18, v19
	v_cvt_pk_fp8_f32 v19, v22, v23
	v_cvt_pk_fp8_f32 v18, v20, v21 op_sel:[0,0,1]
	v_cvt_pk_fp8_f32 v19, v24, v25 op_sel:[0,0,1]
	s_nop 1
	global_store_dwordx2 v117, v[18:19], s[8:9]
	s_waitcnt lgkmcnt(0)
	v_pk_mul_f32 v[26:27], v[26:27], s[26:27] op_sel_hi:[1,0]
	v_pk_mul_f32 v[28:29], v[28:29], s[26:27] op_sel_hi:[1,0]
	v_pk_mul_f32 v[30:31], v[30:31], s[26:27] op_sel_hi:[1,0]
	v_pk_mul_f32 v[32:33], v[32:33], s[26:27] op_sel_hi:[1,0]
	v_cvt_pk_fp8_f32 v26, v26, v27
	v_cvt_pk_fp8_f32 v27, v30, v31
	v_cvt_pk_fp8_f32 v26, v28, v29 op_sel:[0,0,1]
	v_cvt_pk_fp8_f32 v27, v32, v33 op_sel:[0,0,1]
	s_nop 1
	global_store_dwordx2 v118, v[26:27], s[8:9]
	s_add_u32 s8, s8, s23
	s_addc_u32 s9, s9, 0
	s_add_i32 s10, s10, -1
	s_cmp_eq_u32 s10, 0
	s_cbranch_scc1 .Lcvt_phase_done
	global_load_dwordx4 v[2:5], v98, s[6:7]
	global_load_dwordx4 v[6:9], v99, s[6:7]
	global_load_dwordx4 v[10:13], v100, s[6:7]
	global_load_dwordx4 v[14:17], v101, s[6:7]
	global_load_dwordx4 v[18:21], v102, s[6:7]
	global_load_dwordx4 v[22:25], v103, s[6:7]
	global_load_dwordx4 v[26:29], v104, s[6:7]
	global_load_dwordx4 v[30:33], v105, s[6:7]
	s_cmp_lg_u32 s11, 0
	s_cselect_b32 s0, s13, 0
	s_cselect_b32 s1, 1, 0
	s_add_u32 s6, s6, s0
	s_addc_u32 s7, s7, 0
	s_sub_u32 s11, s11, s1
	s_waitcnt vmcnt(32)
	ds_write2_b32 v106, v34, v35 offset1:1
	ds_write2_b32 v106, v36, v37 offset0:2 offset1:3
	ds_write2_b32 v107, v38, v39 offset1:1
	ds_write2_b32 v107, v40, v41 offset0:2 offset1:3
	ds_write2_b32 v108, v42, v43 offset1:1
	ds_write2_b32 v108, v44, v45 offset0:2 offset1:3
	ds_write2_b32 v109, v46, v47 offset1:1
	ds_write2_b32 v109, v48, v49 offset0:2 offset1:3
	ds_write2_b32 v110, v50, v51 offset1:1
	ds_write2_b32 v110, v52, v53 offset0:2 offset1:3
	ds_write2_b32 v111, v54, v55 offset1:1
	ds_write2_b32 v111, v56, v57 offset0:2 offset1:3
	ds_write2_b32 v112, v58, v59 offset1:1
	ds_write2_b32 v112, v60, v61 offset0:2 offset1:3
	ds_write2_b32 v113, v62, v63 offset1:1
	ds_write2_b32 v113, v64, v65 offset0:2 offset1:3
	s_waitcnt lgkmcnt(0)
	ds_read2_b32 v[34:35], v114 offset1:33
	ds_read2_b32 v[36:37], v114 offset0:66 offset1:99
	ds_read2_b32 v[38:39], v114 offset0:132 offset1:165
	ds_read2_b32 v[40:41], v114 offset0:198 offset1:231
	ds_read2_b32 v[42:43], v114 offset0:8 offset1:41
	ds_read2_b32 v[44:45], v114 offset0:74 offset1:107
	ds_read2_b32 v[46:47], v114 offset0:140 offset1:173
	ds_read2_b32 v[48:49], v114 offset0:206 offset1:239
	ds_read2_b32 v[50:51], v114 offset0:16 offset1:49
	ds_read2_b32 v[52:53], v114 offset0:82 offset1:115
	ds_read2_b32 v[54:55], v114 offset0:148 offset1:181
	ds_read2_b32 v[56:57], v114 offset0:214 offset1:247
	ds_read2_b32 v[58:59], v114 offset0:24 offset1:57
	ds_read2_b32 v[60:61], v114 offset0:90 offset1:123
	ds_read2_b32 v[62:63], v114 offset0:156 offset1:189
	ds_read2_b32 v[64:65], v114 offset0:222 offset1:255
	s_waitcnt lgkmcnt(12)
	v_pk_mul_f32 v[34:35], v[34:35], s[26:27] op_sel_hi:[1,0]
	v_pk_mul_f32 v[36:37], v[36:37], s[26:27] op_sel_hi:[1,0]
	v_pk_mul_f32 v[38:39], v[38:39], s[26:27] op_sel_hi:[1,0]
	v_pk_mul_f32 v[40:41], v[40:41], s[26:27] op_sel_hi:[1,0]
	v_cvt_pk_fp8_f32 v34, v34, v35
	v_cvt_pk_fp8_f32 v35, v38, v39
	v_cvt_pk_fp8_f32 v34, v36, v37 op_sel:[0,0,1]
	v_cvt_pk_fp8_f32 v35, v40, v41 op_sel:[0,0,1]
	s_nop 1
	global_store_dwordx2 v115, v[34:35], s[8:9]
	s_waitcnt lgkmcnt(8)
	v_pk_mul_f32 v[42:43], v[42:43], s[26:27] op_sel_hi:[1,0]
	v_pk_mul_f32 v[44:45], v[44:45], s[26:27] op_sel_hi:[1,0]
	v_pk_mul_f32 v[46:47], v[46:47], s[26:27] op_sel_hi:[1,0]
	v_pk_mul_f32 v[48:49], v[48:49], s[26:27] op_sel_hi:[1,0]
	v_cvt_pk_fp8_f32 v42, v42, v43
	v_cvt_pk_fp8_f32 v43, v46, v47
	v_cvt_pk_fp8_f32 v42, v44, v45 op_sel:[0,0,1]
	v_cvt_pk_fp8_f32 v43, v48, v49 op_sel:[0,0,1]
	s_nop 1
	global_store_dwordx2 v116, v[42:43], s[8:9]
	s_waitcnt lgkmcnt(4)
	v_pk_mul_f32 v[50:51], v[50:51], s[26:27] op_sel_hi:[1,0]
	v_pk_mul_f32 v[52:53], v[52:53], s[26:27] op_sel_hi:[1,0]
	v_pk_mul_f32 v[54:55], v[54:55], s[26:27] op_sel_hi:[1,0]
	v_pk_mul_f32 v[56:57], v[56:57], s[26:27] op_sel_hi:[1,0]
	v_cvt_pk_fp8_f32 v50, v50, v51
	v_cvt_pk_fp8_f32 v51, v54, v55
	v_cvt_pk_fp8_f32 v50, v52, v53 op_sel:[0,0,1]
	v_cvt_pk_fp8_f32 v51, v56, v57 op_sel:[0,0,1]
	s_nop 1
	global_store_dwordx2 v117, v[50:51], s[8:9]
	s_waitcnt lgkmcnt(0)
	v_pk_mul_f32 v[58:59], v[58:59], s[26:27] op_sel_hi:[1,0]
	v_pk_mul_f32 v[60:61], v[60:61], s[26:27] op_sel_hi:[1,0]
	v_pk_mul_f32 v[62:63], v[62:63], s[26:27] op_sel_hi:[1,0]
	v_pk_mul_f32 v[64:65], v[64:65], s[26:27] op_sel_hi:[1,0]
	v_cvt_pk_fp8_f32 v58, v58, v59
	v_cvt_pk_fp8_f32 v59, v62, v63
	v_cvt_pk_fp8_f32 v58, v60, v61 op_sel:[0,0,1]
	v_cvt_pk_fp8_f32 v59, v64, v65 op_sel:[0,0,1]
	s_nop 1
	global_store_dwordx2 v118, v[58:59], s[8:9]
	s_add_u32 s8, s8, s23
	s_addc_u32 s9, s9, 0
	s_add_i32 s10, s10, -1
	s_cmp_eq_u32 s10, 0
	s_cbranch_scc1 .Lcvt_phase_done
	global_load_dwordx4 v[34:37], v98, s[6:7]
	global_load_dwordx4 v[38:41], v99, s[6:7]
	global_load_dwordx4 v[42:45], v100, s[6:7]
	global_load_dwordx4 v[46:49], v101, s[6:7]
	global_load_dwordx4 v[50:53], v102, s[6:7]
	global_load_dwordx4 v[54:57], v103, s[6:7]
	global_load_dwordx4 v[58:61], v104, s[6:7]
	global_load_dwordx4 v[62:65], v105, s[6:7]
	s_cmp_lg_u32 s11, 0
	s_cselect_b32 s0, s13, 0
	s_cselect_b32 s1, 1, 0
	s_add_u32 s6, s6, s0
	s_addc_u32 s7, s7, 0
	s_sub_u32 s11, s11, s1
	s_waitcnt vmcnt(32)
	ds_write2_b32 v106, v66, v67 offset1:1
	ds_write2_b32 v106, v68, v69 offset0:2 offset1:3
	ds_write2_b32 v107, v70, v71 offset1:1
	ds_write2_b32 v107, v72, v73 offset0:2 offset1:3
	ds_write2_b32 v108, v74, v75 offset1:1
	ds_write2_b32 v108, v76, v77 offset0:2 offset1:3
	ds_write2_b32 v109, v78, v79 offset1:1
	ds_write2_b32 v109, v80, v81 offset0:2 offset1:3
	ds_write2_b32 v110, v82, v83 offset1:1
	ds_write2_b32 v110, v84, v85 offset0:2 offset1:3
	ds_write2_b32 v111, v86, v87 offset1:1
	ds_write2_b32 v111, v88, v89 offset0:2 offset1:3
	ds_write2_b32 v112, v90, v91 offset1:1
	ds_write2_b32 v112, v92, v93 offset0:2 offset1:3
	ds_write2_b32 v113, v94, v95 offset1:1
	ds_write2_b32 v113, v96, v97 offset0:2 offset1:3
	s_waitcnt lgkmcnt(0)
	ds_read2_b32 v[66:67], v114 offset1:33
	ds_read2_b32 v[68:69], v114 offset0:66 offset1:99
	ds_read2_b32 v[70:71], v114 offset0:132 offset1:165
	ds_read2_b32 v[72:73], v114 offset0:198 offset1:231
	ds_read2_b32 v[74:75], v114 offset0:8 offset1:41
	ds_read2_b32 v[76:77], v114 offset0:74 offset1:107
	ds_read2_b32 v[78:79], v114 offset0:140 offset1:173
	ds_read2_b32 v[80:81], v114 offset0:206 offset1:239
	ds_read2_b32 v[82:83], v114 offset0:16 offset1:49
	ds_read2_b32 v[84:85], v114 offset0:82 offset1:115
	ds_read2_b32 v[86:87], v114 offset0:148 offset1:181
	ds_read2_b32 v[88:89], v114 offset0:214 offset1:247
	ds_read2_b32 v[90:91], v114 offset0:24 offset1:57
	ds_read2_b32 v[92:93], v114 offset0:90 offset1:123
	ds_read2_b32 v[94:95], v114 offset0:156 offset1:189
	ds_read2_b32 v[96:97], v114 offset0:222 offset1:255
	s_waitcnt lgkmcnt(12)
	v_pk_mul_f32 v[66:67], v[66:67], s[26:27] op_sel_hi:[1,0]
	v_pk_mul_f32 v[68:69], v[68:69], s[26:27] op_sel_hi:[1,0]
	v_pk_mul_f32 v[70:71], v[70:71], s[26:27] op_sel_hi:[1,0]
	v_pk_mul_f32 v[72:73], v[72:73], s[26:27] op_sel_hi:[1,0]
	v_cvt_pk_fp8_f32 v66, v66, v67
	v_cvt_pk_fp8_f32 v67, v70, v71
	v_cvt_pk_fp8_f32 v66, v68, v69 op_sel:[0,0,1]
	v_cvt_pk_fp8_f32 v67, v72, v73 op_sel:[0,0,1]
	s_nop 1
	global_store_dwordx2 v115, v[66:67], s[8:9]
	s_waitcnt lgkmcnt(8)
	v_pk_mul_f32 v[74:75], v[74:75], s[26:27] op_sel_hi:[1,0]
	v_pk_mul_f32 v[76:77], v[76:77], s[26:27] op_sel_hi:[1,0]
	v_pk_mul_f32 v[78:79], v[78:79], s[26:27] op_sel_hi:[1,0]
	v_pk_mul_f32 v[80:81], v[80:81], s[26:27] op_sel_hi:[1,0]
	v_cvt_pk_fp8_f32 v74, v74, v75
	v_cvt_pk_fp8_f32 v75, v78, v79
	v_cvt_pk_fp8_f32 v74, v76, v77 op_sel:[0,0,1]
	v_cvt_pk_fp8_f32 v75, v80, v81 op_sel:[0,0,1]
	s_nop 1
	global_store_dwordx2 v116, v[74:75], s[8:9]
	s_waitcnt lgkmcnt(4)
	v_pk_mul_f32 v[82:83], v[82:83], s[26:27] op_sel_hi:[1,0]
	v_pk_mul_f32 v[84:85], v[84:85], s[26:27] op_sel_hi:[1,0]
	v_pk_mul_f32 v[86:87], v[86:87], s[26:27] op_sel_hi:[1,0]
	v_pk_mul_f32 v[88:89], v[88:89], s[26:27] op_sel_hi:[1,0]
	v_cvt_pk_fp8_f32 v82, v82, v83
	v_cvt_pk_fp8_f32 v83, v86, v87
	v_cvt_pk_fp8_f32 v82, v84, v85 op_sel:[0,0,1]
	v_cvt_pk_fp8_f32 v83, v88, v89 op_sel:[0,0,1]
	s_nop 1
	global_store_dwordx2 v117, v[82:83], s[8:9]
	s_waitcnt lgkmcnt(0)
	v_pk_mul_f32 v[90:91], v[90:91], s[26:27] op_sel_hi:[1,0]
	v_pk_mul_f32 v[92:93], v[92:93], s[26:27] op_sel_hi:[1,0]
	v_pk_mul_f32 v[94:95], v[94:95], s[26:27] op_sel_hi:[1,0]
	v_pk_mul_f32 v[96:97], v[96:97], s[26:27] op_sel_hi:[1,0]
	v_cvt_pk_fp8_f32 v90, v90, v91
	v_cvt_pk_fp8_f32 v91, v94, v95
	v_cvt_pk_fp8_f32 v90, v92, v93 op_sel:[0,0,1]
	v_cvt_pk_fp8_f32 v91, v96, v97 op_sel:[0,0,1]
	s_nop 1
	global_store_dwordx2 v118, v[90:91], s[8:9]
	s_add_u32 s8, s8, s23
	s_addc_u32 s9, s9, 0
	s_add_i32 s10, s10, -1
	s_cmp_eq_u32 s10, 0
	s_cbranch_scc1 .Lcvt_phase_done
	global_load_dwordx4 v[66:69], v98, s[6:7]
	global_load_dwordx4 v[70:73], v99, s[6:7]
	global_load_dwordx4 v[74:77], v100, s[6:7]
	global_load_dwordx4 v[78:81], v101, s[6:7]
	global_load_dwordx4 v[82:85], v102, s[6:7]
	global_load_dwordx4 v[86:89], v103, s[6:7]
	global_load_dwordx4 v[90:93], v104, s[6:7]
	global_load_dwordx4 v[94:97], v105, s[6:7]
	s_cmp_lg_u32 s11, 0
	s_cselect_b32 s0, s13, 0
	s_cselect_b32 s1, 1, 0
	s_add_u32 s6, s6, s0
	s_addc_u32 s7, s7, 0
	s_sub_u32 s11, s11, s1
	s_waitcnt vmcnt(32)
	ds_write2_b32 v106, v124, v125 offset1:1
	ds_write2_b32 v106, v126, v127 offset0:2 offset1:3
	ds_write2_b32 v107, v128, v129 offset1:1
	ds_write2_b32 v107, v130, v131 offset0:2 offset1:3
	ds_write2_b32 v108, v132, v133 offset1:1
	ds_write2_b32 v108, v134, v135 offset0:2 offset1:3
	ds_write2_b32 v109, v136, v137 offset1:1
	ds_write2_b32 v109, v138, v139 offset0:2 offset1:3
	ds_write2_b32 v110, v140, v141 offset1:1
	ds_write2_b32 v110, v142, v143 offset0:2 offset1:3
	ds_write2_b32 v111, v144, v145 offset1:1
	ds_write2_b32 v111, v146, v147 offset0:2 offset1:3
	ds_write2_b32 v112, v148, v149 offset1:1
	ds_write2_b32 v112, v150, v151 offset0:2 offset1:3
	ds_write2_b32 v113, v152, v153 offset1:1
	ds_write2_b32 v113, v154, v155 offset0:2 offset1:3
	s_waitcnt lgkmcnt(0)
	ds_read2_b32 v[124:125], v114 offset1:33
	ds_read2_b32 v[126:127], v114 offset0:66 offset1:99
	ds_read2_b32 v[128:129], v114 offset0:132 offset1:165
	ds_read2_b32 v[130:131], v114 offset0:198 offset1:231
	ds_read2_b32 v[132:133], v114 offset0:8 offset1:41
	ds_read2_b32 v[134:135], v114 offset0:74 offset1:107
	ds_read2_b32 v[136:137], v114 offset0:140 offset1:173
	ds_read2_b32 v[138:139], v114 offset0:206 offset1:239
	ds_read2_b32 v[140:141], v114 offset0:16 offset1:49
	ds_read2_b32 v[142:143], v114 offset0:82 offset1:115
	ds_read2_b32 v[144:145], v114 offset0:148 offset1:181
	ds_read2_b32 v[146:147], v114 offset0:214 offset1:247
	ds_read2_b32 v[148:149], v114 offset0:24 offset1:57
	ds_read2_b32 v[150:151], v114 offset0:90 offset1:123
	ds_read2_b32 v[152:153], v114 offset0:156 offset1:189
	ds_read2_b32 v[154:155], v114 offset0:222 offset1:255
	s_waitcnt lgkmcnt(12)
	v_pk_mul_f32 v[124:125], v[124:125], s[26:27] op_sel_hi:[1,0]
	v_pk_mul_f32 v[126:127], v[126:127], s[26:27] op_sel_hi:[1,0]
	v_pk_mul_f32 v[128:129], v[128:129], s[26:27] op_sel_hi:[1,0]
	v_pk_mul_f32 v[130:131], v[130:131], s[26:27] op_sel_hi:[1,0]
	v_cvt_pk_fp8_f32 v124, v124, v125
	v_cvt_pk_fp8_f32 v125, v128, v129
	v_cvt_pk_fp8_f32 v124, v126, v127 op_sel:[0,0,1]
	v_cvt_pk_fp8_f32 v125, v130, v131 op_sel:[0,0,1]
	s_nop 1
	global_store_dwordx2 v115, v[124:125], s[8:9]
	s_waitcnt lgkmcnt(8)
	v_pk_mul_f32 v[132:133], v[132:133], s[26:27] op_sel_hi:[1,0]
	v_pk_mul_f32 v[134:135], v[134:135], s[26:27] op_sel_hi:[1,0]
	v_pk_mul_f32 v[136:137], v[136:137], s[26:27] op_sel_hi:[1,0]
	v_pk_mul_f32 v[138:139], v[138:139], s[26:27] op_sel_hi:[1,0]
	v_cvt_pk_fp8_f32 v132, v132, v133
	v_cvt_pk_fp8_f32 v133, v136, v137
	v_cvt_pk_fp8_f32 v132, v134, v135 op_sel:[0,0,1]
	v_cvt_pk_fp8_f32 v133, v138, v139 op_sel:[0,0,1]
	s_nop 1
	global_store_dwordx2 v116, v[132:133], s[8:9]
	s_waitcnt lgkmcnt(4)
	v_pk_mul_f32 v[140:141], v[140:141], s[26:27] op_sel_hi:[1,0]
	v_pk_mul_f32 v[142:143], v[142:143], s[26:27] op_sel_hi:[1,0]
	v_pk_mul_f32 v[144:145], v[144:145], s[26:27] op_sel_hi:[1,0]
	v_pk_mul_f32 v[146:147], v[146:147], s[26:27] op_sel_hi:[1,0]
	v_cvt_pk_fp8_f32 v140, v140, v141
	v_cvt_pk_fp8_f32 v141, v144, v145
	v_cvt_pk_fp8_f32 v140, v142, v143 op_sel:[0,0,1]
	v_cvt_pk_fp8_f32 v141, v146, v147 op_sel:[0,0,1]
	s_nop 1
	global_store_dwordx2 v117, v[140:141], s[8:9]
	s_waitcnt lgkmcnt(0)
	v_pk_mul_f32 v[148:149], v[148:149], s[26:27] op_sel_hi:[1,0]
	v_pk_mul_f32 v[150:151], v[150:151], s[26:27] op_sel_hi:[1,0]
	v_pk_mul_f32 v[152:153], v[152:153], s[26:27] op_sel_hi:[1,0]
	v_pk_mul_f32 v[154:155], v[154:155], s[26:27] op_sel_hi:[1,0]
	v_cvt_pk_fp8_f32 v148, v148, v149
	v_cvt_pk_fp8_f32 v149, v152, v153
	v_cvt_pk_fp8_f32 v148, v150, v151 op_sel:[0,0,1]
	v_cvt_pk_fp8_f32 v149, v154, v155 op_sel:[0,0,1]
	s_nop 1
	global_store_dwordx2 v118, v[148:149], s[8:9]
	s_add_u32 s8, s8, s23
	s_addc_u32 s9, s9, 0
	s_add_i32 s10, s10, -1
	s_cmp_eq_u32 s10, 0
	s_cbranch_scc1 .Lcvt_phase_done
	global_load_dwordx4 v[124:127], v98, s[6:7]
	global_load_dwordx4 v[128:131], v99, s[6:7]
	global_load_dwordx4 v[132:135], v100, s[6:7]
	global_load_dwordx4 v[136:139], v101, s[6:7]
	global_load_dwordx4 v[140:143], v102, s[6:7]
	global_load_dwordx4 v[144:147], v103, s[6:7]
	global_load_dwordx4 v[148:151], v104, s[6:7]
	global_load_dwordx4 v[152:155], v105, s[6:7]
	s_cmp_lg_u32 s11, 0
	s_cselect_b32 s0, s13, 0
	s_cselect_b32 s1, 1, 0
	s_add_u32 s6, s6, s0
	s_addc_u32 s7, s7, 0
	s_sub_u32 s11, s11, s1
	s_waitcnt vmcnt(32)
	ds_write2_b32 v106, v156, v157 offset1:1
	ds_write2_b32 v106, v158, v159 offset0:2 offset1:3
	ds_write2_b32 v107, v160, v161 offset1:1
	ds_write2_b32 v107, v162, v163 offset0:2 offset1:3
	ds_write2_b32 v108, v164, v165 offset1:1
	ds_write2_b32 v108, v166, v167 offset0:2 offset1:3
	ds_write2_b32 v109, v168, v169 offset1:1
	ds_write2_b32 v109, v170, v171 offset0:2 offset1:3
	ds_write2_b32 v110, v172, v173 offset1:1
	ds_write2_b32 v110, v174, v175 offset0:2 offset1:3
	ds_write2_b32 v111, v176, v177 offset1:1
	ds_write2_b32 v111, v178, v179 offset0:2 offset1:3
	ds_write2_b32 v112, v180, v181 offset1:1
	ds_write2_b32 v112, v182, v183 offset0:2 offset1:3
	ds_write2_b32 v113, v184, v185 offset1:1
	ds_write2_b32 v113, v186, v187 offset0:2 offset1:3
	s_waitcnt lgkmcnt(0)
	ds_read2_b32 v[156:157], v114 offset1:33
	ds_read2_b32 v[158:159], v114 offset0:66 offset1:99
	ds_read2_b32 v[160:161], v114 offset0:132 offset1:165
	ds_read2_b32 v[162:163], v114 offset0:198 offset1:231
	ds_read2_b32 v[164:165], v114 offset0:8 offset1:41
	ds_read2_b32 v[166:167], v114 offset0:74 offset1:107
	ds_read2_b32 v[168:169], v114 offset0:140 offset1:173
	ds_read2_b32 v[170:171], v114 offset0:206 offset1:239
	ds_read2_b32 v[172:173], v114 offset0:16 offset1:49
	ds_read2_b32 v[174:175], v114 offset0:82 offset1:115
	ds_read2_b32 v[176:177], v114 offset0:148 offset1:181
	ds_read2_b32 v[178:179], v114 offset0:214 offset1:247
	ds_read2_b32 v[180:181], v114 offset0:24 offset1:57
	ds_read2_b32 v[182:183], v114 offset0:90 offset1:123
	ds_read2_b32 v[184:185], v114 offset0:156 offset1:189
	ds_read2_b32 v[186:187], v114 offset0:222 offset1:255
	s_waitcnt lgkmcnt(12)
	v_pk_mul_f32 v[156:157], v[156:157], s[26:27] op_sel_hi:[1,0]
	v_pk_mul_f32 v[158:159], v[158:159], s[26:27] op_sel_hi:[1,0]
	v_pk_mul_f32 v[160:161], v[160:161], s[26:27] op_sel_hi:[1,0]
	v_pk_mul_f32 v[162:163], v[162:163], s[26:27] op_sel_hi:[1,0]
	v_cvt_pk_fp8_f32 v156, v156, v157
	v_cvt_pk_fp8_f32 v157, v160, v161
	v_cvt_pk_fp8_f32 v156, v158, v159 op_sel:[0,0,1]
	v_cvt_pk_fp8_f32 v157, v162, v163 op_sel:[0,0,1]
	s_nop 1
	global_store_dwordx2 v115, v[156:157], s[8:9]
	s_waitcnt lgkmcnt(8)
	v_pk_mul_f32 v[164:165], v[164:165], s[26:27] op_sel_hi:[1,0]
	v_pk_mul_f32 v[166:167], v[166:167], s[26:27] op_sel_hi:[1,0]
	v_pk_mul_f32 v[168:169], v[168:169], s[26:27] op_sel_hi:[1,0]
	v_pk_mul_f32 v[170:171], v[170:171], s[26:27] op_sel_hi:[1,0]
	v_cvt_pk_fp8_f32 v164, v164, v165
	v_cvt_pk_fp8_f32 v165, v168, v169
	v_cvt_pk_fp8_f32 v164, v166, v167 op_sel:[0,0,1]
	v_cvt_pk_fp8_f32 v165, v170, v171 op_sel:[0,0,1]
	s_nop 1
	global_store_dwordx2 v116, v[164:165], s[8:9]
	s_waitcnt lgkmcnt(4)
	v_pk_mul_f32 v[172:173], v[172:173], s[26:27] op_sel_hi:[1,0]
	v_pk_mul_f32 v[174:175], v[174:175], s[26:27] op_sel_hi:[1,0]
	v_pk_mul_f32 v[176:177], v[176:177], s[26:27] op_sel_hi:[1,0]
	v_pk_mul_f32 v[178:179], v[178:179], s[26:27] op_sel_hi:[1,0]
	v_cvt_pk_fp8_f32 v172, v172, v173
	v_cvt_pk_fp8_f32 v173, v176, v177
	v_cvt_pk_fp8_f32 v172, v174, v175 op_sel:[0,0,1]
	v_cvt_pk_fp8_f32 v173, v178, v179 op_sel:[0,0,1]
	s_nop 1
	global_store_dwordx2 v117, v[172:173], s[8:9]
	s_waitcnt lgkmcnt(0)
	v_pk_mul_f32 v[180:181], v[180:181], s[26:27] op_sel_hi:[1,0]
	v_pk_mul_f32 v[182:183], v[182:183], s[26:27] op_sel_hi:[1,0]
	v_pk_mul_f32 v[184:185], v[184:185], s[26:27] op_sel_hi:[1,0]
	v_pk_mul_f32 v[186:187], v[186:187], s[26:27] op_sel_hi:[1,0]
	v_cvt_pk_fp8_f32 v180, v180, v181
	v_cvt_pk_fp8_f32 v181, v184, v185
	v_cvt_pk_fp8_f32 v180, v182, v183 op_sel:[0,0,1]
	v_cvt_pk_fp8_f32 v181, v186, v187 op_sel:[0,0,1]
	s_nop 1
	global_store_dwordx2 v118, v[180:181], s[8:9]
	s_add_u32 s8, s8, s23
	s_addc_u32 s9, s9, 0
	s_add_i32 s10, s10, -1
	s_cmp_eq_u32 s10, 0
	s_cbranch_scc1 .Lcvt_phase_done
	s_branch .Lcvt_loop
.Lcvt_phase_done:
	s_waitcnt vmcnt(0)
	s_cmp_eq_u32 s29, 0
	s_cbranch_scc1 .Lcvt_phase1
	s_branch .LBB0_1074
